# GQA unit prologue: tiles 1-2 loads no longer wait for tile 0 to land (full vmcnt drain removed, counted waits remain)
# baseline (speedup 1.0000x reference)
; __device__ __forceinline__ unsigned cvt_pk_bf16(float lo, float hi) { unsigned r; asm volatile("v_cvt_pk_bf16_f32 %0, %1, %2" : "=v"(r) : "v"(lo), "v"(hi)); return r; }
; #define SWAIT() asm volatile("s_waitcnt vmcnt(2)" ::: "memory")
; template <int DQK, bool FIXM> ...
;     ...
;     const bf16_t* Qw = Qp + (size_t)(wid * 32 + r32) * ldq + hi * 8;
; #pragma unroll
;     for (int d0 = 0; d0 < NQ; ++d0) qr[d0] = *(const bf16x8*)(Qw + d0 * 16);
;     if constexpr (DQK == 96) { if (qtok0 >= 0) {
;         const int t = qtok0 + wid * 32 + r32, gr = t >> 6, gc = t & 63;
; #pragma unroll
;         for (int e = 0; e < 2; ++e) { const f32x2* tp = (e == 0) ? rope + gr * 8 + hi * 4 : rope + 2048 + gc * 8 + hi * 4;
;             const f32x4 cs0 = *(const f32x4*)tp, cs1 = *(const f32x4*)(tp + 2);
;             const u32x4 w = __builtin_bit_cast(u32x4, qr[4 + e]); u32x4 o;
;             { const float x1 = bf16lo(w.x), x2 = bf16hi(w.x); o.x = cvt_pk_bf16(x1 * cs0[0] - x2 * cs0[1], x1 * cs0[1] + x2 * cs0[0]); }
;             { const float x1 = bf16lo(w.y), x2 = bf16hi(w.y); o.y = cvt_pk_bf16(x1 * cs0[2] - x2 * cs0[3], x1 * cs0[3] + x2 * cs0[2]); }
;             { const float x1 = bf16lo(w.z), x2 = bf16hi(w.z); o.z = cvt_pk_bf16(x1 * cs1[0] - x2 * cs1[1], x1 * cs1[1] + x2 * cs1[0]); }
;             { const float x1 = bf16lo(w.w), x2 = bf16hi(w.w); o.w = cvt_pk_bf16(x1 * cs1[2] - x2 * cs1[3], x1 * cs1[3] + x2 * cs1[2]); }
;             qr[4 + e] = __builtin_bit_cast(bf16x8, o); } } }
;     const int sr = tid >> 3, c8 = tid & 7, sr2 = (tid >> 2) & 63, c4 = tid & 3;
;     const bool krw = (DQK == 96) && (tid < 256);
;     const int kn_st = B_KN + swz64(sr, c8), v_stw = B_V + v_st(sr, c8 * 8), kr_st = B_KR + swz32(sr2, c4);
;     const unsigned vb0 = (unsigned)(uintptr_t)lds + B_V + v_rd_base(lane);
;     bf16x8 skn[2], sv[2], skr[2];
;     ...
;     f32x16 pA0, pA1, pB0, pB1; float alA, alB; bf16x8 pa0, pa1, pa2, pa3;
;     int bV = 0, bK = BUF, bW = 2 * BUF;
;     ...
;     __syncthreads();
;     SLOAD(0, 0); asm volatile("s_waitcnt vmcnt(0)" ::: "memory"); SWRITE(0, 0);
;     SLOAD(1, 1); if (2 < NT) SLOAD(0, 2);
;     __syncthreads();
;     qkt<DQK>(pA0, pA1, lds, qr, r32, hi, negm);
;     if (FIXM) { alA = 1.f; _Pragma("unroll") for (int r = 0; r < 16; ++r) pA0[r] = __builtin_amdgcn_exp2f(pA0[r]); } else partialSM<true>(pA0, pA1, m_reg, negm, alA);
;     SWAIT(); SWRITEO(BUF, 1);
.LBB0_496:
	s_lshr_b32 s8, s8, 6
	s_and_b64 s[0:1], s[10:11], exec
	s_cselect_b32 s8, s8, s14
	s_and_b32 s9, s8, 7
	s_lshl_b64 s[0:1], s[4:5], 10
	s_add_u32 s0, s15, s0
	s_addc_u32 s1, s16, s1
	s_lshl_b32 s34, s9, 6
	s_lshl_b32 s9, s9, 7
	s_add_u32 s38, s0, s9
	s_addc_u32 s39, s1, 0
	s_lshl_b32 s0, s8, 5
	s_and_b32 s8, s0, 0x80
	s_add_u32 s0, s19, s8
	v_add_u32_e32 v16, s36, v1
	s_addc_u32 s1, s20, 0
	v_ashrrev_i32_e32 v17, 31, v16
	s_add_u32 s8, s23, s8
	v_lshl_add_u64 v[4:5], s[38:39], 0, v[192:193]
	v_lshlrev_b32_e32 v2, 1, v200
	v_lshlrev_b64 v[16:17], 8, v[16:17]
	s_addc_u32 s9, s24, 0
	v_lshl_add_u64 v[4:5], v[4:5], 0, v[2:3]
	v_lshl_add_u64 v[34:35], s[0:1], 0, v[16:17]
	v_lshlrev_b32_e32 v2, 1, v188
	v_lshl_add_u64 v[34:35], v[34:35], 0, v[2:3]
	v_lshl_add_u64 v[16:17], s[8:9], 0, v[16:17]
	global_load_dwordx4 v[114:117], v[4:5], off
	global_load_dwordx4 v[12:15], v[4:5], off offset:32
	global_load_dwordx4 v[8:11], v[4:5], off offset:64
	s_nop 0
	global_load_dwordx4 v[4:7], v[4:5], off offset:96
	s_barrier
	v_lshl_add_u64 v[16:17], v[16:17], 0, v[2:3]
	global_load_dwordx4 v[34:37], v[34:35], off
	s_nop 0
	global_load_dwordx4 v[38:41], v[16:17], off
	s_lshl_b32 s36, s31, 6
	s_sub_i32 s36, s29, s36
	s_and_b64 s[10:11], s[10:11], exec
	s_cselect_b32 s10, s12, s36
	v_add_u32_e32 v16, s10, v191
	v_ashrrev_i32_e32 v17, 31, v16
	v_lshlrev_b64 v[16:17], 8, v[16:17]
	v_add_u32_e32 v42, s10, v189
	v_lshl_add_u64 v[44:45], s[0:1], 0, v[16:17]
	v_lshl_add_u64 v[16:17], s[8:9], 0, v[16:17]
	v_lshl_add_u64 v[44:45], v[44:45], 0, v[2:3]
	v_lshl_add_u64 v[16:17], v[16:17], 0, v[2:3]
	v_ashrrev_i32_e32 v43, 31, v42
	global_load_dwordx4 v[58:61], v[44:45], off
	global_load_dwordx4 v[62:65], v[16:17], off
	v_lshlrev_b64 v[16:17], 8, v[42:43]
	v_lshl_add_u64 v[42:43], s[0:1], 0, v[16:17]
	v_lshl_add_u64 v[16:17], s[8:9], 0, v[16:17]
	v_lshl_add_u64 v[42:43], v[42:43], 0, v[2:3]
	v_lshl_add_u64 v[16:17], v[16:17], 0, v[2:3]
	global_load_dwordx4 v[118:121], v[42:43], off
	global_load_dwordx4 v[122:125], v[16:17], off
	v_add_u32_e32 v106, 0, v187
	v_add_u32_e32 v46, v208, v209
	v_add_u32_e32 v107, 0, v214
	v_add_u32_e32 v16, v208, v210
	v_add_u32_e32 v17, v208, v211
	v_add_u32_e32 v57, v208, v212
	v_mov_b32_e32 v136, 0
	s_mov_b32 s10, 0xa000
	s_movk_i32 s11, 0x5000
	v_mov_b32_e32 v137, v221
	v_mov_b32_e32 v50, 0
	v_mov_b32_e32 v42, v136
	v_mov_b32_e32 v43, v136
	v_mov_b32_e32 v48, v136
	v_mov_b32_e32 v49, v136
	v_mov_b32_e32 v51, v136
	v_mov_b32_e32 v56, v136
	v_lshl_add_u64 v[134:135], s[8:9], 0, v[2:3]
	s_waitcnt vmcnt(5)
	ds_write_b128 v106, v[34:37]
	s_waitcnt vmcnt(4)
	ds_write_b128 v107, v[38:41] offset:12288
	s_waitcnt lgkmcnt(0)
	s_barrier
	ds_read_b128 v[34:37], v46
	ds_read_b128 v[38:41], v46 offset:4096
	s_waitcnt lgkmcnt(1)
	v_mfma_f32_32x32x16_bf16 v[82:97], v[34:37], v[114:117], v[18:33]
	ds_read_b128 v[34:37], v16
	ds_read_b128 v[44:47], v17
	ds_read_b128 v[52:55], v17 offset:4096
	ds_read_b128 v[98:101], v57
	ds_read_b128 v[102:105], v57 offset:4096
	v_mov_b32_e32 v57, v136
	s_waitcnt lgkmcnt(5)
	v_mfma_f32_32x32x16_bf16 v[66:81], v[38:41], v[114:117], v[18:33]
	ds_read_b128 v[38:41], v16 offset:4096
	s_waitcnt vmcnt(2)
	v_lshl_add_u64 v[16:17], s[0:1], 0, v[2:3]
	s_add_i32 s0, s30, -1
	s_waitcnt vmcnt(3)
	ds_write_b128 v106, v[58:61] offset:20480
	s_waitcnt vmcnt(2)
	ds_write_b128 v107, v[62:65] offset:32768
	v_mov_b32_e32 v58, v136
	v_mov_b32_e32 v59, v136
	s_waitcnt lgkmcnt(7)
	v_mfma_f32_32x32x16_bf16 v[82:97], v[34:37], v[12:15], v[82:97]
	v_mov_b32_e32 v34, 0
	v_mov_b32_e32 v35, v136
	v_mov_b32_e32 v36, v136
	v_mov_b32_e32 v37, v136
	v_mov_b32_e32 v60, v136
	v_mov_b32_e32 v61, v136
	v_mov_b32_e32 v62, v136
	s_waitcnt lgkmcnt(2)
	v_mfma_f32_32x32x16_bf16 v[66:81], v[38:41], v[12:15], v[66:81]
	v_mov_b32_e32 v38, v136
	v_mov_b32_e32 v39, v136
	v_mov_b32_e32 v40, v136
	v_mov_b32_e32 v41, v136
	v_mov_b32_e32 v63, v136
	v_mov_b32_e32 v64, v136
	v_mov_b32_e32 v65, v136
	v_mfma_f32_32x32x16_bf16 v[82:97], v[44:47], v[8:11], v[82:97]
	v_mov_b32_e32 v44, v136
	v_mov_b32_e32 v45, v136
	v_mov_b32_e32 v46, v136
	v_mov_b32_e32 v47, v136
	v_mfma_f32_32x32x16_bf16 v[66:81], v[52:55], v[8:11], v[66:81]
	v_mov_b32_e32 v52, v136
	v_mov_b32_e32 v53, v136
	v_mov_b32_e32 v54, v136
	v_mov_b32_e32 v55, v136
	v_mfma_f32_32x32x16_bf16 v[82:97], v[98:101], v[4:7], v[82:97]
	v_mfma_f32_32x32x16_bf16 v[66:81], v[102:105], v[4:7], v[66:81]
	s_nop 10
	v_exp_f32_e32 v143, v82
	v_exp_f32_e32 v145, v83
	v_exp_f32_e32 v141, v84
	v_exp_f32_e32 v144, v85
	v_exp_f32_e32 v139, v86
	v_exp_f32_e32 v142, v87
	v_exp_f32_e32 v138, v88
	v_exp_f32_e32 v140, v89
	v_exp_f32_e32 v151, v90
	v_exp_f32_e32 v153, v91
	v_exp_f32_e32 v149, v92
	v_exp_f32_e32 v152, v93
	v_exp_f32_e32 v147, v94
	v_exp_f32_e32 v150, v95
	v_exp_f32_e32 v146, v96
	v_exp_f32_e32 v148, v97
